# bf16 GEMM unit loops (in-projection, out-projection): first K-iteration peeled with MFMA C=0, 128 accumulator-zeroing v_movs per unit removed
# speedup vs baseline: 1.0029x; 1.0007x over previous
.LBB0_507:
	v_mov_b64_e32 v[2:3], 0x100
	s_ashr_i32 s47, s46, 31
	v_cmp_lt_i64_e32 vcc, s[26:27], v[2:3]
	s_lshl_b64 s[26:27], s[46:47], 19
	s_add_u32 s26, s16, s26
	s_addc_u32 s27, s17, s27
	s_and_b64 s[36:37], vcc, exec
	s_cselect_b32 s47, s27, s51
	s_cselect_b32 s64, s26, s50
	s_ashr_i32 s45, s44, 31
	s_lshl_b64 s[36:37], s[44:45], 19
	s_add_u32 s36, s5, s36
	s_addc_u32 s37, s58, s37
	s_and_b64 s[54:55], vcc, exec
	s_cselect_b32 s45, s37, s53
	s_cselect_b32 s65, s36, s52
	s_add_u32 s50, s50, 0x40080
	s_addc_u32 s51, s51, 0
	s_add_u32 s66, s52, 0x100
	s_addc_u32 s67, s53, 0
	s_mov_b32 s68, -2
	s_add_u32 s4, s50, 0xfffc0080
	s_addc_u32 s52, s51, -1
	s_add_i32 s69, 0, 0x10000
	s_cmp_eq_u32 s68, 12
	s_cselect_b32 s55, s47, s52
	s_cselect_b32 s54, s64, s4
	s_cselect_b32 s53, s45, s67
	s_cselect_b32 s52, s65, s66
	s_add_i32 s4, 0, 0x14000
	v_add_u32_e32 v142, s69, v195
	v_add_u32_e32 v158, s4, v195
	ds_read_b128 v[130:133], v142
	ds_read_b128 v[134:137], v142 offset:1024
	ds_read_b128 v[138:141], v142 offset:2048
	ds_read_b128 v[142:145], v142 offset:3072
	ds_read_b128 v[146:149], v158
	ds_read_b128 v[150:153], v158 offset:1024
	ds_read_b128 v[154:157], v158 offset:2048
	ds_read_b128 v[158:161], v158 offset:3072
	v_lshl_add_u64 v[210:211], s[50:51], 0, v[202:203]
	s_add_i32 m0, s49, 0xc000
	ds_read_b128 v[162:165], v234
	ds_read_b128 v[166:169], v234 offset:1024
	ds_read_b128 v[170:173], v234 offset:2048
	ds_read_b128 v[174:177], v234 offset:3072
	ds_read_b128 v[178:181], v234 offset:4096
	ds_read_b128 v[182:185], v234 offset:5120
	ds_read_b128 v[186:189], v234 offset:6144
	ds_read_b128 v[206:209], v234 offset:7168
	global_load_lds_dwordx4 v[210:211], off
	v_lshl_add_u64 v[210:211], s[50:51], 0, v[204:205]
	s_add_i32 m0, s49, 0xe000
	s_nop 0
	global_load_lds_dwordx4 v[210:211], off
	s_waitcnt vmcnt(8)
	s_waitcnt lgkmcnt(0)
	s_barrier
	s_setprio 1
	s_waitcnt lgkmcnt(0)
	v_mfma_f32_16x16x32_bf16 v[126:129], v[130:133], v[162:165], 0
	v_mfma_f32_16x16x32_bf16 v[122:125], v[138:141], v[162:165], 0
	v_mfma_f32_16x16x32_bf16 v[110:113], v[130:133], v[170:173], 0
	v_mfma_f32_16x16x32_bf16 v[106:109], v[138:141], v[170:173], 0
	v_mfma_f32_16x16x32_bf16 v[98:101], v[130:133], v[178:181], 0
	v_mfma_f32_16x16x32_bf16 v[90:93], v[138:141], v[178:181], 0
	v_mfma_f32_16x16x32_bf16 v[82:85], v[130:133], v[186:189], 0
	v_mfma_f32_16x16x32_bf16 v[74:77], v[138:141], v[186:189], 0
	v_mfma_f32_16x16x32_bf16 v[126:129], v[134:137], v[166:169], v[126:129]
	v_mfma_f32_16x16x32_bf16 v[122:125], v[142:145], v[166:169], v[122:125]
	v_mfma_f32_16x16x32_bf16 v[110:113], v[134:137], v[174:177], v[110:113]
	v_mfma_f32_16x16x32_bf16 v[106:109], v[142:145], v[174:177], v[106:109]
	v_mfma_f32_16x16x32_bf16 v[98:101], v[134:137], v[182:185], v[98:101]
	v_mfma_f32_16x16x32_bf16 v[90:93], v[142:145], v[182:185], v[90:93]
	v_mfma_f32_16x16x32_bf16 v[82:85], v[134:137], v[206:209], v[82:85]
	v_mfma_f32_16x16x32_bf16 v[74:77], v[142:145], v[206:209], v[74:77]
	s_setprio 0
	s_setprio 1
	v_mfma_f32_16x16x32_bf16 v[118:121], v[146:149], v[162:165], 0
	v_mfma_f32_16x16x32_bf16 v[114:117], v[154:157], v[162:165], 0
	v_mfma_f32_16x16x32_bf16 v[102:105], v[146:149], v[170:173], 0
	v_mfma_f32_16x16x32_bf16 v[94:97], v[154:157], v[170:173], 0
	v_mfma_f32_16x16x32_bf16 v[86:89], v[146:149], v[178:181], 0
	v_mfma_f32_16x16x32_bf16 v[78:81], v[154:157], v[178:181], 0
	v_mfma_f32_16x16x32_bf16 v[70:73], v[146:149], v[186:189], 0
	v_mfma_f32_16x16x32_bf16 v[66:69], v[154:157], v[186:189], 0
	v_mfma_f32_16x16x32_bf16 v[118:121], v[150:153], v[166:169], v[118:121]
	v_mfma_f32_16x16x32_bf16 v[114:117], v[158:161], v[166:169], v[114:117]
	v_mfma_f32_16x16x32_bf16 v[102:105], v[150:153], v[174:177], v[102:105]
	v_mfma_f32_16x16x32_bf16 v[94:97], v[158:161], v[174:177], v[94:97]
	v_mfma_f32_16x16x32_bf16 v[86:89], v[150:153], v[182:185], v[86:89]
	v_mfma_f32_16x16x32_bf16 v[78:81], v[158:161], v[182:185], v[78:81]
	v_mfma_f32_16x16x32_bf16 v[70:73], v[150:153], v[206:209], v[70:73]
	v_mfma_f32_16x16x32_bf16 v[66:69], v[158:161], v[206:209], v[66:69]
	s_setprio 0
	s_barrier
	s_add_i32 s69, s69, s59
	v_lshl_add_u64 v[210:211], s[52:53], 0, v[0:1]
	s_mov_b32 m0, s69
	ds_read_b128 v[162:165], v234 offset:16384
	ds_read_b128 v[166:169], v234 offset:17408
	ds_read_b128 v[170:173], v234 offset:18432
	ds_read_b128 v[174:177], v234 offset:19456
	ds_read_b128 v[178:181], v234 offset:20480
	ds_read_b128 v[182:185], v234 offset:21504
	ds_read_b128 v[186:189], v234 offset:22528
	ds_read_b128 v[206:209], v234 offset:23552
	global_load_lds_dwordx4 v[210:211], off
	s_add_i32 m0, s69, 0x2000
	s_add_u32 s70, s52, 0x40000
	v_lshl_add_u64 v[212:213], s[52:53], 0, v[200:201]
	s_addc_u32 s71, s53, 0
	s_add_i32 s4, s4, s59
	global_load_lds_dwordx4 v[212:213], off
	v_lshl_add_u64 v[214:215], s[70:71], 0, v[0:1]
	s_mov_b32 m0, s4
	v_lshl_add_u64 v[216:217], s[54:55], 0, v[198:199]
	global_load_lds_dwordx4 v[214:215], off
	v_lshl_add_u64 v[214:215], s[70:71], 0, v[200:201]
	s_add_i32 m0, s4, 0x2000
	s_nop 0
	global_load_lds_dwordx4 v[214:215], off
	v_lshl_add_u64 v[214:215], s[54:55], 0, v[196:197]
	s_mov_b32 m0, s49
	s_nop 0
	global_load_lds_dwordx4 v[214:215], off
	s_mov_b32 m0, s30
	s_nop 0
	global_load_lds_dwordx4 v[216:217], off
	s_waitcnt vmcnt(8)
	s_waitcnt lgkmcnt(0)
	s_barrier
	s_setprio 1
	s_waitcnt lgkmcnt(0)
	v_mfma_f32_16x16x32_bf16 v[62:65], v[130:133], v[162:165], 0
	v_mfma_f32_16x16x32_bf16 v[58:61], v[138:141], v[162:165], 0
	v_mfma_f32_16x16x32_bf16 v[50:53], v[130:133], v[170:173], 0
	v_mfma_f32_16x16x32_bf16 v[42:45], v[138:141], v[170:173], 0
	v_mfma_f32_16x16x32_bf16 v[34:37], v[130:133], v[178:181], 0
	v_mfma_f32_16x16x32_bf16 v[26:29], v[138:141], v[178:181], 0
	v_mfma_f32_16x16x32_bf16 v[18:21], v[130:133], v[186:189], 0
	v_mfma_f32_16x16x32_bf16 v[10:13], v[138:141], v[186:189], 0
	v_mfma_f32_16x16x32_bf16 v[62:65], v[134:137], v[166:169], v[62:65]
	v_mfma_f32_16x16x32_bf16 v[58:61], v[142:145], v[166:169], v[58:61]
	v_mfma_f32_16x16x32_bf16 v[50:53], v[134:137], v[174:177], v[50:53]
	v_mfma_f32_16x16x32_bf16 v[42:45], v[142:145], v[174:177], v[42:45]
	v_mfma_f32_16x16x32_bf16 v[34:37], v[134:137], v[182:185], v[34:37]
	v_mfma_f32_16x16x32_bf16 v[26:29], v[142:145], v[182:185], v[26:29]
	v_mfma_f32_16x16x32_bf16 v[18:21], v[134:137], v[206:209], v[18:21]
	v_mfma_f32_16x16x32_bf16 v[10:13], v[142:145], v[206:209], v[10:13]
	s_setprio 0
	s_setprio 1
	v_mfma_f32_16x16x32_bf16 v[54:57], v[146:149], v[162:165], 0
	v_mfma_f32_16x16x32_bf16 v[46:49], v[154:157], v[162:165], 0
	v_mfma_f32_16x16x32_bf16 v[38:41], v[146:149], v[170:173], 0
	v_mfma_f32_16x16x32_bf16 v[30:33], v[154:157], v[170:173], 0
	v_mfma_f32_16x16x32_bf16 v[22:25], v[146:149], v[178:181], 0
	v_mfma_f32_16x16x32_bf16 v[14:17], v[154:157], v[178:181], 0
	v_mfma_f32_16x16x32_bf16 v[6:9], v[146:149], v[186:189], 0
	v_mfma_f32_16x16x32_bf16 v[2:5], v[154:157], v[186:189], 0
	v_mfma_f32_16x16x32_bf16 v[54:57], v[150:153], v[166:169], v[54:57]
	v_mfma_f32_16x16x32_bf16 v[46:49], v[158:161], v[166:169], v[46:49]
	v_mfma_f32_16x16x32_bf16 v[38:41], v[150:153], v[174:177], v[38:41]
	v_mfma_f32_16x16x32_bf16 v[30:33], v[158:161], v[174:177], v[30:33]
	v_mfma_f32_16x16x32_bf16 v[22:25], v[150:153], v[182:185], v[22:25]
	v_mfma_f32_16x16x32_bf16 v[14:17], v[158:161], v[182:185], v[14:17]
	v_mfma_f32_16x16x32_bf16 v[6:9], v[150:153], v[206:209], v[6:9]
	v_mfma_f32_16x16x32_bf16 v[2:5], v[158:161], v[206:209], v[2:5]
	s_setprio 0
	s_barrier
	s_add_i32 s4, 0, 0x18000
	s_add_i32 s69, 0, 0x1c000
	v_add_u32_e32 v142, s4, v195
	v_add_u32_e32 v158, s69, v195
	ds_read_b128 v[130:133], v142
	ds_read_b128 v[134:137], v142 offset:1024
	ds_read_b128 v[138:141], v142 offset:2048
	ds_read_b128 v[142:145], v142 offset:3072
	ds_read_b128 v[146:149], v158
	ds_read_b128 v[150:153], v158 offset:1024
	ds_read_b128 v[154:157], v158 offset:2048
	ds_read_b128 v[158:161], v158 offset:3072
	s_add_u32 s54, s54, 0x40000
	s_addc_u32 s55, s55, 0
	s_mov_b32 m0, s31
	v_lshl_add_u64 v[218:219], s[54:55], 0, v[196:197]
	ds_read_b128 v[162:165], v234 offset:32768
	ds_read_b128 v[166:169], v234 offset:33792
	ds_read_b128 v[170:173], v234 offset:34816
	ds_read_b128 v[174:177], v234 offset:35840
	ds_read_b128 v[178:181], v234 offset:36864
	ds_read_b128 v[182:185], v234 offset:37888
	ds_read_b128 v[186:189], v234 offset:38912
	ds_read_b128 v[206:209], v234 offset:39936
	global_load_lds_dwordx4 v[218:219], off
	v_lshl_add_u64 v[218:219], s[54:55], 0, v[198:199]
	s_mov_b32 m0, s60
	s_nop 0
	global_load_lds_dwordx4 v[218:219], off
	s_waitcnt vmcnt(8)
	s_waitcnt lgkmcnt(0)
	s_barrier
	s_setprio 1
	s_waitcnt lgkmcnt(0)
	v_mfma_f32_16x16x32_bf16 v[126:129], v[130:133], v[162:165], v[126:129]
	v_mfma_f32_16x16x32_bf16 v[122:125], v[138:141], v[162:165], v[122:125]
	v_mfma_f32_16x16x32_bf16 v[110:113], v[130:133], v[170:173], v[110:113]
	v_mfma_f32_16x16x32_bf16 v[106:109], v[138:141], v[170:173], v[106:109]
	v_mfma_f32_16x16x32_bf16 v[98:101], v[130:133], v[178:181], v[98:101]
	v_mfma_f32_16x16x32_bf16 v[90:93], v[138:141], v[178:181], v[90:93]
	v_mfma_f32_16x16x32_bf16 v[82:85], v[130:133], v[186:189], v[82:85]
	v_mfma_f32_16x16x32_bf16 v[74:77], v[138:141], v[186:189], v[74:77]
	v_mfma_f32_16x16x32_bf16 v[126:129], v[134:137], v[166:169], v[126:129]
	v_mfma_f32_16x16x32_bf16 v[122:125], v[142:145], v[166:169], v[122:125]
	v_mfma_f32_16x16x32_bf16 v[110:113], v[134:137], v[174:177], v[110:113]
	v_mfma_f32_16x16x32_bf16 v[106:109], v[142:145], v[174:177], v[106:109]
	v_mfma_f32_16x16x32_bf16 v[98:101], v[134:137], v[182:185], v[98:101]
	v_mfma_f32_16x16x32_bf16 v[90:93], v[142:145], v[182:185], v[90:93]
	v_mfma_f32_16x16x32_bf16 v[82:85], v[134:137], v[206:209], v[82:85]
	v_mfma_f32_16x16x32_bf16 v[74:77], v[142:145], v[206:209], v[74:77]
	s_setprio 0
	s_setprio 1
	v_mfma_f32_16x16x32_bf16 v[118:121], v[146:149], v[162:165], v[118:121]
	v_mfma_f32_16x16x32_bf16 v[114:117], v[154:157], v[162:165], v[114:117]
	v_mfma_f32_16x16x32_bf16 v[102:105], v[146:149], v[170:173], v[102:105]
	v_mfma_f32_16x16x32_bf16 v[94:97], v[154:157], v[170:173], v[94:97]
	v_mfma_f32_16x16x32_bf16 v[86:89], v[146:149], v[178:181], v[86:89]
	v_mfma_f32_16x16x32_bf16 v[78:81], v[154:157], v[178:181], v[78:81]
	v_mfma_f32_16x16x32_bf16 v[70:73], v[146:149], v[186:189], v[70:73]
	v_mfma_f32_16x16x32_bf16 v[66:69], v[154:157], v[186:189], v[66:69]
	v_mfma_f32_16x16x32_bf16 v[118:121], v[150:153], v[166:169], v[118:121]
	v_mfma_f32_16x16x32_bf16 v[114:117], v[158:161], v[166:169], v[114:117]
	v_mfma_f32_16x16x32_bf16 v[102:105], v[150:153], v[174:177], v[102:105]
	v_mfma_f32_16x16x32_bf16 v[94:97], v[158:161], v[174:177], v[94:97]
	v_mfma_f32_16x16x32_bf16 v[86:89], v[150:153], v[182:185], v[86:89]
	v_mfma_f32_16x16x32_bf16 v[78:81], v[158:161], v[182:185], v[78:81]
	v_mfma_f32_16x16x32_bf16 v[70:73], v[150:153], v[206:209], v[70:73]
	v_mfma_f32_16x16x32_bf16 v[66:69], v[158:161], v[206:209], v[66:69]
	s_setprio 0
	s_barrier
	s_add_i32 s4, s4, s59
	v_lshl_add_u64 v[210:211], v[210:211], 0, s[22:23]
	s_mov_b32 m0, s4
	ds_read_b128 v[162:165], v234 offset:49152
	ds_read_b128 v[166:169], v234 offset:50176
	ds_read_b128 v[170:173], v234 offset:51200
	ds_read_b128 v[174:177], v234 offset:52224
	ds_read_b128 v[178:181], v234 offset:53248
	ds_read_b128 v[182:185], v234 offset:54272
	ds_read_b128 v[186:189], v234 offset:55296
	ds_read_b128 v[206:209], v234 offset:56320
	global_load_lds_dwordx4 v[210:211], off
	s_add_i32 m0, s4, 0x2000
	s_add_u32 s52, s52, 0x40080
	v_lshl_add_u64 v[210:211], v[212:213], 0, s[22:23]
	s_addc_u32 s53, s53, 0
	s_add_i32 s4, s69, s59
	global_load_lds_dwordx4 v[210:211], off
	v_lshl_add_u64 v[210:211], s[52:53], 0, v[0:1]
	s_mov_b32 m0, s4
	s_nop 0
	global_load_lds_dwordx4 v[210:211], off
	v_lshl_add_u64 v[210:211], s[52:53], 0, v[200:201]
	s_add_i32 m0, s4, 0x2000
	s_nop 0
	global_load_lds_dwordx4 v[210:211], off
	v_lshl_add_u64 v[210:211], v[214:215], 0, s[22:23]
	s_mov_b32 m0, s62
	s_nop 0
	global_load_lds_dwordx4 v[210:211], off
	v_lshl_add_u64 v[210:211], v[216:217], 0, s[22:23]
	s_mov_b32 m0, s63
	s_nop 0
	global_load_lds_dwordx4 v[210:211], off
	s_waitcnt vmcnt(8)
	s_waitcnt lgkmcnt(0)
	s_barrier
	s_setprio 1
	s_waitcnt lgkmcnt(0)
	v_mfma_f32_16x16x32_bf16 v[62:65], v[130:133], v[162:165], v[62:65]
	v_mfma_f32_16x16x32_bf16 v[58:61], v[138:141], v[162:165], v[58:61]
	v_mfma_f32_16x16x32_bf16 v[50:53], v[130:133], v[170:173], v[50:53]
	v_mfma_f32_16x16x32_bf16 v[42:45], v[138:141], v[170:173], v[42:45]
	v_mfma_f32_16x16x32_bf16 v[34:37], v[130:133], v[178:181], v[34:37]
	v_mfma_f32_16x16x32_bf16 v[26:29], v[138:141], v[178:181], v[26:29]
	v_mfma_f32_16x16x32_bf16 v[18:21], v[130:133], v[186:189], v[18:21]
	v_mfma_f32_16x16x32_bf16 v[10:13], v[138:141], v[186:189], v[10:13]
	v_mfma_f32_16x16x32_bf16 v[62:65], v[134:137], v[166:169], v[62:65]
	v_mfma_f32_16x16x32_bf16 v[58:61], v[142:145], v[166:169], v[58:61]
	v_mfma_f32_16x16x32_bf16 v[50:53], v[134:137], v[174:177], v[50:53]
	v_mfma_f32_16x16x32_bf16 v[42:45], v[142:145], v[174:177], v[42:45]
	v_mfma_f32_16x16x32_bf16 v[34:37], v[134:137], v[182:185], v[34:37]
	v_mfma_f32_16x16x32_bf16 v[26:29], v[142:145], v[182:185], v[26:29]
	v_mfma_f32_16x16x32_bf16 v[18:21], v[134:137], v[206:209], v[18:21]
	v_mfma_f32_16x16x32_bf16 v[10:13], v[142:145], v[206:209], v[10:13]
	s_setprio 0
	s_setprio 1
	v_mfma_f32_16x16x32_bf16 v[54:57], v[146:149], v[162:165], v[54:57]
	v_mfma_f32_16x16x32_bf16 v[46:49], v[154:157], v[162:165], v[46:49]
	v_mfma_f32_16x16x32_bf16 v[38:41], v[146:149], v[170:173], v[38:41]
	v_mfma_f32_16x16x32_bf16 v[30:33], v[154:157], v[170:173], v[30:33]
	v_mfma_f32_16x16x32_bf16 v[22:25], v[146:149], v[178:181], v[22:25]
	v_mfma_f32_16x16x32_bf16 v[14:17], v[154:157], v[178:181], v[14:17]
	v_mfma_f32_16x16x32_bf16 v[6:9], v[146:149], v[186:189], v[6:9]
	v_mfma_f32_16x16x32_bf16 v[2:5], v[154:157], v[186:189], v[2:5]
	v_mfma_f32_16x16x32_bf16 v[54:57], v[150:153], v[166:169], v[54:57]
	v_mfma_f32_16x16x32_bf16 v[46:49], v[158:161], v[166:169], v[46:49]
	v_mfma_f32_16x16x32_bf16 v[38:41], v[150:153], v[174:177], v[38:41]
	v_mfma_f32_16x16x32_bf16 v[30:33], v[158:161], v[174:177], v[30:33]
	v_mfma_f32_16x16x32_bf16 v[22:25], v[150:153], v[182:185], v[22:25]
	v_mfma_f32_16x16x32_bf16 v[14:17], v[158:161], v[182:185], v[14:17]
	v_mfma_f32_16x16x32_bf16 v[6:9], v[150:153], v[206:209], v[6:9]
	v_mfma_f32_16x16x32_bf16 v[2:5], v[158:161], v[206:209], v[2:5]
	s_setprio 0
	s_barrier
	s_add_i32 s68, s68, 2
	s_add_u32 s50, s50, 0x100
	s_addc_u32 s51, s51, 0
	s_add_u32 s66, s66, 0x100
	s_addc_u32 s67, s67, 0

.LBB0_672:
	s_ashr_i32 s57, s56, 31
	s_lshl_b64 s[58:59], s[56:57], 19
	s_add_u32 s58, s15, s58
	s_addc_u32 s59, s16, s59
	s_and_b64 s[60:61], s[38:39], exec
	s_cselect_b32 s6, s59, s37
	s_cselect_b32 s27, s58, s36
	s_ashr_i32 s55, s54, 31
	s_lshl_b64 s[60:61], s[54:55], 19
	s_add_u32 s60, s17, s60
	s_addc_u32 s61, s66, s61
	s_and_b64 s[64:65], s[38:39], exec
	s_cselect_b32 s55, s61, s63
	s_cselect_b32 s57, s60, s62
	s_add_u32 s36, s36, 0x40080
	s_addc_u32 s37, s37, 0
	s_add_u32 s74, s62, 0x100
	s_addc_u32 s84, s63, 0
	s_mov_b32 s85, -2
	s_add_u32 s62, s36, 0xfffc0080
	s_addc_u32 s63, s37, -1
	s_add_i32 s86, 0, 0x10000
	s_cmp_eq_u32 s85, 12
	s_cselect_b32 s65, s6, s63
	s_cselect_b32 s64, s27, s62
	v_add_u32_e32 v0, s86, v208
	s_cselect_b32 s63, s55, s84
	s_cselect_b32 s62, s57, s74
	s_add_i32 s87, 0, 0x14000
	ds_read_b128 v[130:133], v0
	ds_read_b128 v[134:137], v0 offset:1024
	ds_read_b128 v[138:141], v0 offset:2048
	ds_read_b128 v[142:145], v0 offset:3072
	v_add_u32_e32 v0, s87, v208
	ds_read_b128 v[146:149], v0
	ds_read_b128 v[150:153], v0 offset:1024
	ds_read_b128 v[154:157], v0 offset:2048
	ds_read_b128 v[158:161], v0 offset:3072
	v_lshl_add_u64 v[202:203], s[36:37], 0, v[172:173]
	s_add_i32 m0, s68, 0xc000
	ds_read_b128 v[184:187], v210
	ds_read_b128 v[198:201], v210 offset:1024
	ds_read_b128 v[212:215], v210 offset:2048
	ds_read_b128 v[216:219], v210 offset:3072
	ds_read_b128 v[220:223], v210 offset:4096
	ds_read_b128 v[234:237], v210 offset:5120
	ds_read_b128 v[238:241], v210 offset:6144
	ds_read_b128 v[242:245], v210 offset:7168
	global_load_lds_dwordx4 v[202:203], off
	v_lshl_add_u64 v[202:203], s[36:37], 0, v[174:175]
	s_add_i32 m0, s68, 0xe000
	s_nop 0
	global_load_lds_dwordx4 v[202:203], off
	s_waitcnt vmcnt(8)
	s_waitcnt lgkmcnt(0)
	s_barrier
	s_setprio 1
	s_waitcnt lgkmcnt(0)
	v_mfma_f32_16x16x32_bf16 v[126:129], v[130:133], v[184:187], 0
	v_mfma_f32_16x16x32_bf16 v[122:125], v[138:141], v[184:187], 0
	v_mfma_f32_16x16x32_bf16 v[118:121], v[130:133], v[212:215], 0
	v_mfma_f32_16x16x32_bf16 v[114:117], v[138:141], v[212:215], 0
	v_mfma_f32_16x16x32_bf16 v[94:97], v[130:133], v[220:223], 0
	v_mfma_f32_16x16x32_bf16 v[90:93], v[138:141], v[220:223], 0
	v_mfma_f32_16x16x32_bf16 v[86:89], v[130:133], v[238:241], 0
	v_mfma_f32_16x16x32_bf16 v[82:85], v[138:141], v[238:241], 0
	v_mfma_f32_16x16x32_bf16 v[126:129], v[134:137], v[198:201], v[126:129]
	v_mfma_f32_16x16x32_bf16 v[122:125], v[142:145], v[198:201], v[122:125]
	v_mfma_f32_16x16x32_bf16 v[118:121], v[134:137], v[216:219], v[118:121]
	v_mfma_f32_16x16x32_bf16 v[114:117], v[142:145], v[216:219], v[114:117]
	v_mfma_f32_16x16x32_bf16 v[94:97], v[134:137], v[234:237], v[94:97]
	v_mfma_f32_16x16x32_bf16 v[90:93], v[142:145], v[234:237], v[90:93]
	v_mfma_f32_16x16x32_bf16 v[86:89], v[134:137], v[242:245], v[86:89]
	v_mfma_f32_16x16x32_bf16 v[82:85], v[142:145], v[242:245], v[82:85]
	s_setprio 0
	s_setprio 1
	v_mfma_f32_16x16x32_bf16 v[110:113], v[146:149], v[184:187], 0
	v_mfma_f32_16x16x32_bf16 v[106:109], v[154:157], v[184:187], 0
	v_mfma_f32_16x16x32_bf16 v[102:105], v[146:149], v[212:215], 0
	v_mfma_f32_16x16x32_bf16 v[98:101], v[154:157], v[212:215], 0
	v_mfma_f32_16x16x32_bf16 v[78:81], v[146:149], v[220:223], 0
	v_mfma_f32_16x16x32_bf16 v[74:77], v[154:157], v[220:223], 0
	v_mfma_f32_16x16x32_bf16 v[70:73], v[146:149], v[238:241], 0
	v_mfma_f32_16x16x32_bf16 v[66:69], v[154:157], v[238:241], 0
	v_mfma_f32_16x16x32_bf16 v[110:113], v[150:153], v[198:201], v[110:113]
	v_mfma_f32_16x16x32_bf16 v[106:109], v[158:161], v[198:201], v[106:109]
	v_mfma_f32_16x16x32_bf16 v[102:105], v[150:153], v[216:219], v[102:105]
	v_mfma_f32_16x16x32_bf16 v[98:101], v[158:161], v[216:219], v[98:101]
	v_mfma_f32_16x16x32_bf16 v[78:81], v[150:153], v[234:237], v[78:81]
	v_mfma_f32_16x16x32_bf16 v[74:77], v[158:161], v[234:237], v[74:77]
	v_mfma_f32_16x16x32_bf16 v[70:73], v[150:153], v[242:245], v[70:73]
	v_mfma_f32_16x16x32_bf16 v[66:69], v[158:161], v[242:245], v[66:69]
	s_setprio 0
	s_barrier
	s_add_i32 s86, s86, s67
	v_lshl_add_u64 v[202:203], s[62:63], 0, v[166:167]
	s_mov_b32 m0, s86
	ds_read_b128 v[184:187], v210 offset:16384
	ds_read_b128 v[198:201], v210 offset:17408
	ds_read_b128 v[212:215], v210 offset:18432
	ds_read_b128 v[216:219], v210 offset:19456
	ds_read_b128 v[220:223], v210 offset:20480
	ds_read_b128 v[234:237], v210 offset:21504
	ds_read_b128 v[238:241], v210 offset:22528
	ds_read_b128 v[242:245], v210 offset:23552
	global_load_lds_dwordx4 v[202:203], off
	s_add_i32 m0, s86, 0x2000
	s_add_u32 s92, s62, 0x40000
	v_lshl_add_u64 v[246:247], s[62:63], 0, v[170:171]
	s_addc_u32 s93, s63, 0
	s_add_i32 s86, s87, s67
	global_load_lds_dwordx4 v[246:247], off
	v_lshl_add_u64 v[248:249], s[92:93], 0, v[166:167]
	s_mov_b32 m0, s86
	v_lshl_add_u64 v[250:251], s[64:65], 0, v[168:169]
	global_load_lds_dwordx4 v[248:249], off
	v_lshl_add_u64 v[248:249], s[92:93], 0, v[170:171]
	s_add_i32 m0, s86, 0x2000
	s_nop 0
	global_load_lds_dwordx4 v[248:249], off
	v_lshl_add_u64 v[248:249], s[64:65], 0, v[164:165]
	s_mov_b32 m0, s68
	s_nop 0
	global_load_lds_dwordx4 v[248:249], off
	s_mov_b32 m0, s69
	s_nop 0
	global_load_lds_dwordx4 v[250:251], off
	s_waitcnt vmcnt(8)
	s_waitcnt lgkmcnt(0)
	s_barrier
	s_setprio 1
	s_waitcnt lgkmcnt(0)
	v_mfma_f32_16x16x32_bf16 v[62:65], v[130:133], v[184:187], 0
	v_mfma_f32_16x16x32_bf16 v[58:61], v[138:141], v[184:187], 0
	v_mfma_f32_16x16x32_bf16 v[54:57], v[130:133], v[212:215], 0
	v_mfma_f32_16x16x32_bf16 v[50:53], v[138:141], v[212:215], 0
	v_mfma_f32_16x16x32_bf16 v[30:33], v[130:133], v[220:223], 0
	v_mfma_f32_16x16x32_bf16 v[26:29], v[138:141], v[220:223], 0
	v_mfma_f32_16x16x32_bf16 v[22:25], v[130:133], v[238:241], 0
	v_mfma_f32_16x16x32_bf16 v[18:21], v[138:141], v[238:241], 0
	v_mfma_f32_16x16x32_bf16 v[62:65], v[134:137], v[198:201], v[62:65]
	v_mfma_f32_16x16x32_bf16 v[58:61], v[142:145], v[198:201], v[58:61]
	v_mfma_f32_16x16x32_bf16 v[54:57], v[134:137], v[216:219], v[54:57]
	v_mfma_f32_16x16x32_bf16 v[50:53], v[142:145], v[216:219], v[50:53]
	v_mfma_f32_16x16x32_bf16 v[30:33], v[134:137], v[234:237], v[30:33]
	v_mfma_f32_16x16x32_bf16 v[26:29], v[142:145], v[234:237], v[26:29]
	v_mfma_f32_16x16x32_bf16 v[22:25], v[134:137], v[242:245], v[22:25]
	v_mfma_f32_16x16x32_bf16 v[18:21], v[142:145], v[242:245], v[18:21]
	s_setprio 0
	s_setprio 1
	v_mfma_f32_16x16x32_bf16 v[46:49], v[146:149], v[184:187], 0
	v_mfma_f32_16x16x32_bf16 v[42:45], v[154:157], v[184:187], 0
	v_mfma_f32_16x16x32_bf16 v[38:41], v[146:149], v[212:215], 0
	v_mfma_f32_16x16x32_bf16 v[34:37], v[154:157], v[212:215], 0
	v_mfma_f32_16x16x32_bf16 v[14:17], v[146:149], v[220:223], 0
	v_mfma_f32_16x16x32_bf16 v[10:13], v[154:157], v[220:223], 0
	v_mfma_f32_16x16x32_bf16 v[6:9], v[146:149], v[238:241], 0
	v_mfma_f32_16x16x32_bf16 v[2:5], v[154:157], v[238:241], 0
	v_mfma_f32_16x16x32_bf16 v[46:49], v[150:153], v[198:201], v[46:49]
	v_mfma_f32_16x16x32_bf16 v[42:45], v[158:161], v[198:201], v[42:45]
	v_mfma_f32_16x16x32_bf16 v[38:41], v[150:153], v[216:219], v[38:41]
	v_mfma_f32_16x16x32_bf16 v[34:37], v[158:161], v[216:219], v[34:37]
	v_mfma_f32_16x16x32_bf16 v[14:17], v[150:153], v[234:237], v[14:17]
	v_mfma_f32_16x16x32_bf16 v[10:13], v[158:161], v[234:237], v[10:13]
	v_mfma_f32_16x16x32_bf16 v[6:9], v[150:153], v[242:245], v[6:9]
	v_mfma_f32_16x16x32_bf16 v[2:5], v[158:161], v[242:245], v[2:5]
	s_setprio 0
	s_barrier
	s_add_i32 s86, 0, 0x18000
	v_add_u32_e32 v0, s86, v208
	s_add_i32 s87, 0, 0x1c000
	ds_read_b128 v[130:133], v0
	ds_read_b128 v[134:137], v0 offset:1024
	ds_read_b128 v[138:141], v0 offset:2048
	ds_read_b128 v[142:145], v0 offset:3072
	v_add_u32_e32 v0, s87, v208
	ds_read_b128 v[146:149], v0
	ds_read_b128 v[150:153], v0 offset:1024
	ds_read_b128 v[154:157], v0 offset:2048
	ds_read_b128 v[158:161], v0 offset:3072
	s_add_u32 s64, s64, 0x40000
	s_addc_u32 s65, s65, 0
	s_mov_b32 m0, s70
	v_lshl_add_u64 v[230:231], s[64:65], 0, v[164:165]
	ds_read_b128 v[184:187], v210 offset:32768
	ds_read_b128 v[198:201], v210 offset:33792
	ds_read_b128 v[212:215], v210 offset:34816
	ds_read_b128 v[216:219], v210 offset:35840
	ds_read_b128 v[220:223], v210 offset:36864
	ds_read_b128 v[234:237], v210 offset:37888
	ds_read_b128 v[238:241], v210 offset:38912
	ds_read_b128 v[242:245], v210 offset:39936
	global_load_lds_dwordx4 v[230:231], off
	v_lshl_add_u64 v[230:231], s[64:65], 0, v[168:169]
	s_mov_b32 m0, s71
	s_nop 0
	global_load_lds_dwordx4 v[230:231], off
	s_waitcnt vmcnt(8)
	s_waitcnt lgkmcnt(0)
	s_barrier
	s_setprio 1
	s_waitcnt lgkmcnt(0)
	v_mfma_f32_16x16x32_bf16 v[126:129], v[130:133], v[184:187], v[126:129]
	v_mfma_f32_16x16x32_bf16 v[122:125], v[138:141], v[184:187], v[122:125]
	v_mfma_f32_16x16x32_bf16 v[118:121], v[130:133], v[212:215], v[118:121]
	v_mfma_f32_16x16x32_bf16 v[114:117], v[138:141], v[212:215], v[114:117]
	v_mfma_f32_16x16x32_bf16 v[94:97], v[130:133], v[220:223], v[94:97]
	v_mfma_f32_16x16x32_bf16 v[90:93], v[138:141], v[220:223], v[90:93]
	v_mfma_f32_16x16x32_bf16 v[86:89], v[130:133], v[238:241], v[86:89]
	v_mfma_f32_16x16x32_bf16 v[82:85], v[138:141], v[238:241], v[82:85]
	v_mfma_f32_16x16x32_bf16 v[126:129], v[134:137], v[198:201], v[126:129]
	v_mfma_f32_16x16x32_bf16 v[122:125], v[142:145], v[198:201], v[122:125]
	v_mfma_f32_16x16x32_bf16 v[118:121], v[134:137], v[216:219], v[118:121]
	v_mfma_f32_16x16x32_bf16 v[114:117], v[142:145], v[216:219], v[114:117]
	v_mfma_f32_16x16x32_bf16 v[94:97], v[134:137], v[234:237], v[94:97]
	v_mfma_f32_16x16x32_bf16 v[90:93], v[142:145], v[234:237], v[90:93]
	v_mfma_f32_16x16x32_bf16 v[86:89], v[134:137], v[242:245], v[86:89]
	v_mfma_f32_16x16x32_bf16 v[82:85], v[142:145], v[242:245], v[82:85]
	s_setprio 0
	s_setprio 1
	v_mfma_f32_16x16x32_bf16 v[110:113], v[146:149], v[184:187], v[110:113]
	v_mfma_f32_16x16x32_bf16 v[106:109], v[154:157], v[184:187], v[106:109]
	v_mfma_f32_16x16x32_bf16 v[102:105], v[146:149], v[212:215], v[102:105]
	v_mfma_f32_16x16x32_bf16 v[98:101], v[154:157], v[212:215], v[98:101]
	v_mfma_f32_16x16x32_bf16 v[78:81], v[146:149], v[220:223], v[78:81]
	v_mfma_f32_16x16x32_bf16 v[74:77], v[154:157], v[220:223], v[74:77]
	v_mfma_f32_16x16x32_bf16 v[70:73], v[146:149], v[238:241], v[70:73]
	v_mfma_f32_16x16x32_bf16 v[66:69], v[154:157], v[238:241], v[66:69]
	v_mfma_f32_16x16x32_bf16 v[110:113], v[150:153], v[198:201], v[110:113]
	v_mfma_f32_16x16x32_bf16 v[106:109], v[158:161], v[198:201], v[106:109]
	v_mfma_f32_16x16x32_bf16 v[102:105], v[150:153], v[216:219], v[102:105]
	v_mfma_f32_16x16x32_bf16 v[98:101], v[158:161], v[216:219], v[98:101]
	v_mfma_f32_16x16x32_bf16 v[78:81], v[150:153], v[234:237], v[78:81]
	v_mfma_f32_16x16x32_bf16 v[74:77], v[158:161], v[234:237], v[74:77]
	v_mfma_f32_16x16x32_bf16 v[70:73], v[150:153], v[242:245], v[70:73]
	v_mfma_f32_16x16x32_bf16 v[66:69], v[158:161], v[242:245], v[66:69]
	s_setprio 0
	s_barrier
	s_add_i32 s64, s86, s67
	v_lshl_add_u64 v[202:203], v[202:203], 0, s[22:23]
	s_mov_b32 m0, s64
	ds_read_b128 v[184:187], v210 offset:49152
	ds_read_b128 v[198:201], v210 offset:50176
	ds_read_b128 v[212:215], v210 offset:51200
	ds_read_b128 v[216:219], v210 offset:52224
	ds_read_b128 v[220:223], v210 offset:53248
	ds_read_b128 v[234:237], v210 offset:54272
	ds_read_b128 v[238:241], v210 offset:55296
	ds_read_b128 v[242:245], v210 offset:56320
	global_load_lds_dwordx4 v[202:203], off
	s_add_i32 m0, s64, 0x2000
	s_add_u32 s62, s62, 0x40080
	v_lshl_add_u64 v[202:203], v[246:247], 0, s[22:23]
	s_addc_u32 s63, s63, 0
	s_add_i32 s64, s87, s67
	global_load_lds_dwordx4 v[202:203], off
	v_lshl_add_u64 v[202:203], s[62:63], 0, v[166:167]
	s_mov_b32 m0, s64
	s_nop 0
	global_load_lds_dwordx4 v[202:203], off
	v_lshl_add_u64 v[202:203], s[62:63], 0, v[170:171]
	s_add_i32 m0, s64, 0x2000
	s_nop 0
	global_load_lds_dwordx4 v[202:203], off
	v_lshl_add_u64 v[202:203], v[248:249], 0, s[22:23]
	s_mov_b32 m0, s78
	s_nop 0
	global_load_lds_dwordx4 v[202:203], off
	v_lshl_add_u64 v[202:203], v[250:251], 0, s[22:23]
	s_mov_b32 m0, s79
	s_nop 0
	global_load_lds_dwordx4 v[202:203], off
	s_waitcnt vmcnt(8)
	s_waitcnt lgkmcnt(0)
	s_barrier
	s_setprio 1
	s_waitcnt lgkmcnt(0)
	v_mfma_f32_16x16x32_bf16 v[62:65], v[130:133], v[184:187], v[62:65]
	v_mfma_f32_16x16x32_bf16 v[58:61], v[138:141], v[184:187], v[58:61]
	v_mfma_f32_16x16x32_bf16 v[54:57], v[130:133], v[212:215], v[54:57]
	v_mfma_f32_16x16x32_bf16 v[50:53], v[138:141], v[212:215], v[50:53]
	v_mfma_f32_16x16x32_bf16 v[30:33], v[130:133], v[220:223], v[30:33]
	v_mfma_f32_16x16x32_bf16 v[26:29], v[138:141], v[220:223], v[26:29]
	v_mfma_f32_16x16x32_bf16 v[22:25], v[130:133], v[238:241], v[22:25]
	v_mfma_f32_16x16x32_bf16 v[18:21], v[138:141], v[238:241], v[18:21]
	v_mfma_f32_16x16x32_bf16 v[62:65], v[134:137], v[198:201], v[62:65]
	v_mfma_f32_16x16x32_bf16 v[58:61], v[142:145], v[198:201], v[58:61]
	v_mfma_f32_16x16x32_bf16 v[54:57], v[134:137], v[216:219], v[54:57]
	v_mfma_f32_16x16x32_bf16 v[50:53], v[142:145], v[216:219], v[50:53]
	v_mfma_f32_16x16x32_bf16 v[30:33], v[134:137], v[234:237], v[30:33]
	v_mfma_f32_16x16x32_bf16 v[26:29], v[142:145], v[234:237], v[26:29]
	v_mfma_f32_16x16x32_bf16 v[22:25], v[134:137], v[242:245], v[22:25]
	v_mfma_f32_16x16x32_bf16 v[18:21], v[142:145], v[242:245], v[18:21]
	s_setprio 0
	s_setprio 1
	v_mfma_f32_16x16x32_bf16 v[46:49], v[146:149], v[184:187], v[46:49]
	v_mfma_f32_16x16x32_bf16 v[42:45], v[154:157], v[184:187], v[42:45]
	v_mfma_f32_16x16x32_bf16 v[38:41], v[146:149], v[212:215], v[38:41]
	v_mfma_f32_16x16x32_bf16 v[34:37], v[154:157], v[212:215], v[34:37]
	v_mfma_f32_16x16x32_bf16 v[14:17], v[146:149], v[220:223], v[14:17]
	v_mfma_f32_16x16x32_bf16 v[10:13], v[154:157], v[220:223], v[10:13]
	v_mfma_f32_16x16x32_bf16 v[6:9], v[146:149], v[238:241], v[6:9]
	v_mfma_f32_16x16x32_bf16 v[2:5], v[154:157], v[238:241], v[2:5]
	v_mfma_f32_16x16x32_bf16 v[46:49], v[150:153], v[198:201], v[46:49]
	v_mfma_f32_16x16x32_bf16 v[42:45], v[158:161], v[198:201], v[42:45]
	v_mfma_f32_16x16x32_bf16 v[38:41], v[150:153], v[216:219], v[38:41]
	v_mfma_f32_16x16x32_bf16 v[34:37], v[158:161], v[216:219], v[34:37]
	v_mfma_f32_16x16x32_bf16 v[14:17], v[150:153], v[234:237], v[14:17]
	v_mfma_f32_16x16x32_bf16 v[10:13], v[158:161], v[234:237], v[10:13]
	v_mfma_f32_16x16x32_bf16 v[6:9], v[150:153], v[242:245], v[6:9]
	v_mfma_f32_16x16x32_bf16 v[2:5], v[158:161], v[242:245], v[2:5]
	s_setprio 0
	s_barrier
	s_add_i32 s85, s85, 2
	s_add_u32 s36, s36, 0x100
	s_addc_u32 s37, s37, 0
	s_add_u32 s74, s74, 0x100
	s_addc_u32 s84, s84, 0
